# baseline (speedup 1.0000x reference)
.LBB5_134:
	s_or_b64 exec, exec, s[12:13]
	v_mov_b32_e32 v1, 0
	s_and_b64 vcc, exec, s[0:1]
	v_lshlrev_b32_e32 v131, 2, v131
	s_cbranch_vccnz .LBB5_138
	v_mov_b32_e32 v0, 0x23e90
	ds_read_b64 v[30:31], v0
	v_mov_b32_e32 v38, 0x3000
	v_lshl_or_b32 v165, v128, 4, v38
	v_mov_b32_e32 v38, 0x9000
	v_lshl_or_b32 v164, v128, 3, v38
	v_or_b32_e32 v166, 0x23900, v131
	v_lshlrev_b32_e32 v167, 2, v127
	v_or_b32_e32 v167, 0x23b00, v167
	v_mov_b32_e32 v94, 0xf149f2ca
	ds_read_b128 v[42:45], v166 offset:768
	ds_read_b128 v[50:53], v166 offset:832
	ds_read_b128 v[58:61], v166 offset:896
	ds_read_b128 v[66:69], v166 offset:960
	ds_read_b128 v[38:41], v166
	ds_read_b128 v[132:135], v165
	ds_read_b128 v[136:139], v165 offset:1024
	ds_read_b128 v[46:49], v166 offset:256
	ds_read_b128 v[140:143], v165 offset:8192
	ds_read_b128 v[144:147], v165 offset:9216
	s_waitcnt lgkmcnt(10)
	v_pk_add_f32 v[0:1], v[120:121], v[30:31] op_sel_hi:[1,0] neg_lo:[0,1] neg_hi:[0,1]
	v_pk_add_f32 v[32:33], v[122:123], v[30:31] op_sel_hi:[1,0] neg_lo:[0,1] neg_hi:[0,1]
	v_pk_mul_f32 v[0:1], v[30:31], v[0:1] op_sel:[1,0]
	v_pk_mul_f32 v[32:33], v[30:31], v[32:33] op_sel:[1,0]
	v_pk_fma_f32 v[84:85], v[70:71], v[0:1], v[102:103]
	v_pk_fma_f32 v[0:1], v[72:73], v[32:33], v[104:105]
	v_pk_add_f32 v[32:33], v[118:119], v[30:31] op_sel_hi:[1,0] neg_lo:[0,1] neg_hi:[0,1]
	v_pk_mul_f32 v[32:33], v[30:31], v[32:33] op_sel:[1,0]
	v_pk_fma_f32 v[118:119], v[74:75], v[32:33], v[106:107]
	v_pk_add_f32 v[32:33], v[124:125], v[30:31] op_sel_hi:[1,0] neg_lo:[0,1] neg_hi:[0,1]
	v_pk_mul_f32 v[32:33], v[30:31], v[32:33] op_sel:[1,0]
	v_pk_fma_f32 v[124:125], v[76:77], v[32:33], v[108:109]
	v_pk_add_f32 v[32:33], v[116:117], v[30:31] op_sel_hi:[1,0] neg_lo:[0,1] neg_hi:[0,1]
	v_pk_mul_f32 v[32:33], v[30:31], v[32:33] op_sel:[1,0]
	v_pk_fma_f32 v[116:117], v[96:97], v[32:33], v[86:87]
	v_pk_add_f32 v[32:33], v[114:115], v[30:31] op_sel_hi:[1,0] neg_lo:[0,1] neg_hi:[0,1]
	v_cvt_pk_bf16_f32 v34, v116, v117
	v_pk_mul_f32 v[32:33], v[30:31], v[32:33] op_sel:[1,0]
	v_cmp_eq_u32_e32 vcc, 3, v126
	v_pk_fma_f32 v[114:115], v[152:153], v[32:33], v[88:89]
	v_pk_add_f32 v[32:33], v[110:111], v[30:31] op_sel_hi:[1,0] neg_lo:[0,1] neg_hi:[0,1]
	v_cvt_pk_bf16_f32 v35, v114, v115
	v_pk_mul_f32 v[32:33], v[30:31], v[32:33] op_sel:[1,0]
	v_pk_fma_f32 v[110:111], v[90:91], v[32:33], v[98:99]
	v_pk_add_f32 v[32:33], v[112:113], v[30:31] op_sel_hi:[1,0] neg_lo:[0,1] neg_hi:[0,1]
	v_cvt_pk_bf16_f32 v36, v110, v111
	v_pk_mul_f32 v[30:31], v[30:31], v[32:33] op_sel:[1,0]
	v_cvt_pk_bf16_f32 v32, v118, v119
	v_pk_fma_f32 v[112:113], v[92:93], v[30:31], v[100:101]
	v_cvt_pk_bf16_f32 v30, v84, v85
	v_cvt_pk_bf16_f32 v31, v0, v1
	v_cvt_pk_bf16_f32 v33, v124, v125
	v_cvt_pk_bf16_f32 v37, v112, v113
	s_waitcnt lgkmcnt(0)
	ds_read_b32 v95, v167
	ds_read_b128 v[148:151], v165 offset:16384
	ds_read_b128 v[154:157], v165 offset:17408
	ds_read_b64 v[158:159], v164
	ds_read_b64 v[160:161], v164 offset:2048
	ds_read_b64 v[162:163], v164 offset:4096
	ds_read_b64 v[64:65], v164 offset:6144
	s_waitcnt lgkmcnt(4)
	v_mov_b32_e32 v54, v95
	v_mov_b32_e32 v55, v95
	v_mov_b32_e32 v56, v95
	v_mov_b32_e32 v57, v95
	v_mfma_f32_16x16x32_bf16 v[38:41], v[132:135], v[30:33], v[38:41]
	v_mfma_f32_16x16x32_bf16 v[46:49], v[140:143], v[30:33], v[46:49]
	v_mfma_f32_16x16x32_bf16 v[54:57], v[30:33], v[148:151], v[54:57]
	v_mfma_f32_16x16x32_bf16 v[38:41], v[136:139], v[34:37], v[38:41]
	v_mfma_f32_16x16x32_bf16 v[46:49], v[144:147], v[34:37], v[46:49]
	v_mfma_f32_16x16x32_bf16 v[54:57], v[34:37], v[154:157], v[54:57]
	ds_read_b128 v[132:135], v165 offset:2048
	ds_read_b128 v[136:139], v165 offset:3072
	ds_read_b128 v[140:143], v165 offset:10240
	ds_read_b128 v[144:147], v165 offset:11264
	ds_read_b128 v[148:151], v165 offset:18432
	ds_read_b128 v[154:157], v165 offset:19456
	ds_read_b32 v95, v167 offset:64
	v_cvt_pk_bf16_f32 v74, v38, v39
	v_cvt_pk_bf16_f32 v75, v40, v41
	v_cvt_pk_bf16_f32 v76, v46, v47
	v_cvt_pk_bf16_f32 v77, v48, v49
	ds_read_b128 v[38:41], v166 offset:64
	ds_read_b128 v[46:49], v166 offset:320
	v_mfma_f32_16x16x16_bf16 v[70:73], v[76:77], v[74:75], 0
	v_cvt_pk_bf16_f32 v86, v54, v55
	v_cvt_pk_bf16_f32 v87, v56, v57
	s_nop 5
	v_max_f32_e32 v88, v72, v73
	v_max3_f32 v88, v70, v71, v88
	v_cndmask_b32_e32 v88, v88, v94, vcc
	v_mov_b32_e32 v89, v88
	s_nop 1
	v_permlane16_swap_b32_e32 v88, v89
	v_max_f32_e32 v88, v88, v89
	v_mov_b32_e32 v89, v88
	s_nop 1
	v_permlane32_swap_b32_e32 v88, v89
	v_max_f32_e32 v88, v88, v89
	v_sub_f32_e32 v70, v70, v88
	v_sub_f32_e32 v71, v71, v88
	v_sub_f32_e32 v72, v72, v88
	v_sub_f32_e32 v73, v73, v88
	v_mul_f32_e32 v70, 0x3fb8aa3b, v70
	v_mul_f32_e32 v71, 0x3fb8aa3b, v71
	v_mul_f32_e32 v72, 0x3fb8aa3b, v72
	v_mul_f32_e32 v73, 0x3fb8aa3b, v73
	v_exp_f32_e32 v70, v70
	v_exp_f32_e32 v71, v71
	v_exp_f32_e32 v72, v72
	v_exp_f32_e32 v73, v73
	s_nop 0
	v_cndmask_b32_e64 v70, v70, 0, vcc
	v_cndmask_b32_e64 v71, v71, 0, vcc
	v_cndmask_b32_e64 v72, v72, 0, vcc
	v_cndmask_b32_e64 v73, v73, 0, vcc
	v_add_f32_e32 v90, v70, v71
	v_add_f32_e32 v91, v72, v73
	v_add_f32_e32 v90, v90, v91
	v_cvt_pk_bf16_f32 v92, v70, v71
	v_cvt_pk_bf16_f32 v93, v72, v73
	v_mov_b32_e32 v91, v90
	s_nop 1
	v_permlane16_swap_b32_e32 v90, v91
	v_add_f32_e32 v90, v90, v91
	v_mfma_f32_16x16x16_bf16 v[70:73], v[86:87], v[92:93], 0
	v_mov_b32_e32 v91, v90
	s_nop 1
	v_permlane32_swap_b32_e32 v90, v91
	v_add_f32_e32 v90, v90, v91
	v_rcp_f32_e32 v90, v90
	s_nop 2
	v_mul_f32_e32 v70, v70, v90
	v_mul_f32_e32 v71, v71, v90
	v_mul_f32_e32 v72, v72, v90
	v_mul_f32_e32 v73, v73, v90
	v_cvt_pk_bf16_f32 v92, v70, v71
	v_cvt_pk_bf16_f32 v93, v72, v73
	s_waitcnt lgkmcnt(9)
	s_nop 0
	v_mfma_f32_16x16x16_bf16 v[42:45], v[158:159], v[92:93], v[42:45]
	v_mfma_f32_16x16x16_bf16 v[50:53], v[160:161], v[92:93], v[50:53]
	v_mfma_f32_16x16x16_bf16 v[58:61], v[162:163], v[92:93], v[58:61]
	v_mfma_f32_16x16x16_bf16 v[66:69], v[64:65], v[92:93], v[66:69]
	ds_read_b64 v[158:159], v164 offset:512
	ds_read_b64 v[160:161], v164 offset:2560
	ds_read_b64 v[162:163], v164 offset:4608
	ds_read_b64 v[64:65], v164 offset:6656
	s_waitcnt lgkmcnt(4)
	v_mov_b32_e32 v54, v95
	v_mov_b32_e32 v55, v95
	v_mov_b32_e32 v56, v95
	v_mov_b32_e32 v57, v95
	v_mfma_f32_16x16x32_bf16 v[38:41], v[132:135], v[30:33], v[38:41]
	v_mfma_f32_16x16x32_bf16 v[46:49], v[140:143], v[30:33], v[46:49]
	v_mfma_f32_16x16x32_bf16 v[54:57], v[30:33], v[148:151], v[54:57]
	v_mfma_f32_16x16x32_bf16 v[38:41], v[136:139], v[34:37], v[38:41]
	v_mfma_f32_16x16x32_bf16 v[46:49], v[144:147], v[34:37], v[46:49]
	v_mfma_f32_16x16x32_bf16 v[54:57], v[34:37], v[154:157], v[54:57]
	ds_read_b128 v[132:135], v165 offset:4096
	ds_read_b128 v[136:139], v165 offset:5120
	ds_read_b128 v[140:143], v165 offset:12288
	ds_read_b128 v[144:147], v165 offset:13312
	ds_read_b128 v[148:151], v165 offset:20480
	ds_read_b128 v[154:157], v165 offset:21504
	ds_read_b32 v95, v167 offset:128
	v_cvt_pk_bf16_f32 v74, v38, v39
	v_cvt_pk_bf16_f32 v75, v40, v41
	v_cvt_pk_bf16_f32 v76, v46, v47
	v_cvt_pk_bf16_f32 v77, v48, v49
	ds_read_b128 v[38:41], v166 offset:128
	ds_read_b128 v[46:49], v166 offset:384
	v_mfma_f32_16x16x16_bf16 v[70:73], v[76:77], v[74:75], 0
	v_cvt_pk_bf16_f32 v86, v54, v55
	v_cvt_pk_bf16_f32 v87, v56, v57
	s_nop 5
	v_max_f32_e32 v88, v72, v73
	v_max3_f32 v88, v70, v71, v88
	v_cndmask_b32_e32 v88, v88, v94, vcc
	v_mov_b32_e32 v89, v88
	s_nop 1
	v_permlane16_swap_b32_e32 v88, v89
	v_max_f32_e32 v88, v88, v89
	v_mov_b32_e32 v89, v88
	s_nop 1
	v_permlane32_swap_b32_e32 v88, v89
	v_max_f32_e32 v88, v88, v89
	v_sub_f32_e32 v70, v70, v88
	v_sub_f32_e32 v71, v71, v88
	v_sub_f32_e32 v72, v72, v88
	v_sub_f32_e32 v73, v73, v88
	v_mul_f32_e32 v70, 0x3fb8aa3b, v70
	v_mul_f32_e32 v71, 0x3fb8aa3b, v71
	v_mul_f32_e32 v72, 0x3fb8aa3b, v72
	v_mul_f32_e32 v73, 0x3fb8aa3b, v73
	v_exp_f32_e32 v70, v70
	v_exp_f32_e32 v71, v71
	v_exp_f32_e32 v72, v72
	v_exp_f32_e32 v73, v73
	s_nop 0
	v_cndmask_b32_e64 v70, v70, 0, vcc
	v_cndmask_b32_e64 v71, v71, 0, vcc
	v_cndmask_b32_e64 v72, v72, 0, vcc
	v_cndmask_b32_e64 v73, v73, 0, vcc
	v_add_f32_e32 v90, v70, v71
	v_add_f32_e32 v91, v72, v73
	v_add_f32_e32 v90, v90, v91
	v_cvt_pk_bf16_f32 v92, v70, v71
	v_cvt_pk_bf16_f32 v93, v72, v73
	v_mov_b32_e32 v91, v90
	s_nop 1
	v_permlane16_swap_b32_e32 v90, v91
	v_add_f32_e32 v90, v90, v91
	v_mfma_f32_16x16x16_bf16 v[70:73], v[86:87], v[92:93], 0
	v_mov_b32_e32 v91, v90
	s_nop 1
	v_permlane32_swap_b32_e32 v90, v91
	v_add_f32_e32 v90, v90, v91
	v_rcp_f32_e32 v90, v90
	s_nop 2
	v_mul_f32_e32 v70, v70, v90
	v_mul_f32_e32 v71, v71, v90
	v_mul_f32_e32 v72, v72, v90
	v_mul_f32_e32 v73, v73, v90
	v_cvt_pk_bf16_f32 v92, v70, v71
	v_cvt_pk_bf16_f32 v93, v72, v73
	s_waitcnt lgkmcnt(9)
	s_nop 0
	v_mfma_f32_16x16x16_bf16 v[42:45], v[158:159], v[92:93], v[42:45]
	v_mfma_f32_16x16x16_bf16 v[50:53], v[160:161], v[92:93], v[50:53]
	v_mfma_f32_16x16x16_bf16 v[58:61], v[162:163], v[92:93], v[58:61]
	v_mfma_f32_16x16x16_bf16 v[66:69], v[64:65], v[92:93], v[66:69]
	ds_read_b64 v[158:159], v164 offset:1024
	ds_read_b64 v[160:161], v164 offset:3072
	ds_read_b64 v[162:163], v164 offset:5120
	ds_read_b64 v[64:65], v164 offset:7168
	s_waitcnt lgkmcnt(4)
	v_mov_b32_e32 v54, v95
	v_mov_b32_e32 v55, v95
	v_mov_b32_e32 v56, v95
	v_mov_b32_e32 v57, v95
	v_mfma_f32_16x16x32_bf16 v[38:41], v[132:135], v[30:33], v[38:41]
	v_mfma_f32_16x16x32_bf16 v[46:49], v[140:143], v[30:33], v[46:49]
	v_mfma_f32_16x16x32_bf16 v[54:57], v[30:33], v[148:151], v[54:57]
	v_mfma_f32_16x16x32_bf16 v[38:41], v[136:139], v[34:37], v[38:41]
	v_mfma_f32_16x16x32_bf16 v[46:49], v[144:147], v[34:37], v[46:49]
	v_mfma_f32_16x16x32_bf16 v[54:57], v[34:37], v[154:157], v[54:57]
	ds_read_b128 v[132:135], v165 offset:6144
	ds_read_b128 v[136:139], v165 offset:7168
	ds_read_b128 v[140:143], v165 offset:14336
	ds_read_b128 v[144:147], v165 offset:15360
	ds_read_b128 v[148:151], v165 offset:22528
	ds_read_b128 v[154:157], v165 offset:23552
	ds_read_b32 v95, v167 offset:192
	v_cvt_pk_bf16_f32 v74, v38, v39
	v_cvt_pk_bf16_f32 v75, v40, v41
	v_cvt_pk_bf16_f32 v76, v46, v47
	v_cvt_pk_bf16_f32 v77, v48, v49
	ds_read_b128 v[38:41], v166 offset:192
	ds_read_b128 v[46:49], v166 offset:448
	v_mfma_f32_16x16x16_bf16 v[70:73], v[76:77], v[74:75], 0
	v_cvt_pk_bf16_f32 v86, v54, v55
	v_cvt_pk_bf16_f32 v87, v56, v57
	s_nop 5
	v_max_f32_e32 v88, v72, v73
	v_max3_f32 v88, v70, v71, v88
	v_cndmask_b32_e32 v88, v88, v94, vcc
	v_mov_b32_e32 v89, v88
	s_nop 1
	v_permlane16_swap_b32_e32 v88, v89
	v_max_f32_e32 v88, v88, v89
	v_mov_b32_e32 v89, v88
	s_nop 1
	v_permlane32_swap_b32_e32 v88, v89
	v_max_f32_e32 v88, v88, v89
	v_sub_f32_e32 v70, v70, v88
	v_sub_f32_e32 v71, v71, v88
	v_sub_f32_e32 v72, v72, v88
	v_sub_f32_e32 v73, v73, v88
	v_mul_f32_e32 v70, 0x3fb8aa3b, v70
	v_mul_f32_e32 v71, 0x3fb8aa3b, v71
	v_mul_f32_e32 v72, 0x3fb8aa3b, v72
	v_mul_f32_e32 v73, 0x3fb8aa3b, v73
	v_exp_f32_e32 v70, v70
	v_exp_f32_e32 v71, v71
	v_exp_f32_e32 v72, v72
	v_exp_f32_e32 v73, v73
	s_nop 0
	v_cndmask_b32_e64 v70, v70, 0, vcc
	v_cndmask_b32_e64 v71, v71, 0, vcc
	v_cndmask_b32_e64 v72, v72, 0, vcc
	v_cndmask_b32_e64 v73, v73, 0, vcc
	v_add_f32_e32 v90, v70, v71
	v_add_f32_e32 v91, v72, v73
	v_add_f32_e32 v90, v90, v91
	v_cvt_pk_bf16_f32 v92, v70, v71
	v_cvt_pk_bf16_f32 v93, v72, v73
	v_mov_b32_e32 v91, v90
	s_nop 1
	v_permlane16_swap_b32_e32 v90, v91
	v_add_f32_e32 v90, v90, v91
	v_mfma_f32_16x16x16_bf16 v[70:73], v[86:87], v[92:93], 0
	v_mov_b32_e32 v91, v90
	s_nop 1
	v_permlane32_swap_b32_e32 v90, v91
	v_add_f32_e32 v90, v90, v91
	v_rcp_f32_e32 v90, v90
	s_nop 2
	v_mul_f32_e32 v70, v70, v90
	v_mul_f32_e32 v71, v71, v90
	v_mul_f32_e32 v72, v72, v90
	v_mul_f32_e32 v73, v73, v90
	v_cvt_pk_bf16_f32 v92, v70, v71
	v_cvt_pk_bf16_f32 v93, v72, v73
	s_waitcnt lgkmcnt(9)
	s_nop 0
	v_mfma_f32_16x16x16_bf16 v[42:45], v[158:159], v[92:93], v[42:45]
	v_mfma_f32_16x16x16_bf16 v[50:53], v[160:161], v[92:93], v[50:53]
	v_mfma_f32_16x16x16_bf16 v[58:61], v[162:163], v[92:93], v[58:61]
	v_mfma_f32_16x16x16_bf16 v[66:69], v[64:65], v[92:93], v[66:69]
	ds_read_b64 v[158:159], v164 offset:1536
	ds_read_b64 v[160:161], v164 offset:3584
	ds_read_b64 v[162:163], v164 offset:5632
	ds_read_b64 v[64:65], v164 offset:7680
	s_waitcnt lgkmcnt(4)
	v_mov_b32_e32 v54, v95
	v_mov_b32_e32 v55, v95
	v_mov_b32_e32 v56, v95
	v_mov_b32_e32 v57, v95
	v_mfma_f32_16x16x32_bf16 v[38:41], v[132:135], v[30:33], v[38:41]
	v_mfma_f32_16x16x32_bf16 v[46:49], v[140:143], v[30:33], v[46:49]
	v_mfma_f32_16x16x32_bf16 v[54:57], v[30:33], v[148:151], v[54:57]
	v_mfma_f32_16x16x32_bf16 v[38:41], v[136:139], v[34:37], v[38:41]
	v_mfma_f32_16x16x32_bf16 v[46:49], v[144:147], v[34:37], v[46:49]
	v_mfma_f32_16x16x32_bf16 v[54:57], v[34:37], v[154:157], v[54:57]
	s_nop 6
	v_cvt_pk_bf16_f32 v74, v38, v39
	v_cvt_pk_bf16_f32 v75, v40, v41
	v_cvt_pk_bf16_f32 v76, v46, v47
	v_cvt_pk_bf16_f32 v77, v48, v49
	s_nop 1
	v_mfma_f32_16x16x16_bf16 v[70:73], v[76:77], v[74:75], 0
	v_cvt_pk_bf16_f32 v86, v54, v55
	v_cvt_pk_bf16_f32 v87, v56, v57
	s_nop 5
	v_max_f32_e32 v88, v72, v73
	v_max3_f32 v88, v70, v71, v88
	v_cndmask_b32_e32 v88, v88, v94, vcc
	v_mov_b32_e32 v89, v88
	s_nop 1
	v_permlane16_swap_b32_e32 v88, v89
	v_max_f32_e32 v88, v88, v89
	v_mov_b32_e32 v89, v88
	s_nop 1
	v_permlane32_swap_b32_e32 v88, v89
	v_max_f32_e32 v88, v88, v89
	v_sub_f32_e32 v70, v70, v88
	v_sub_f32_e32 v71, v71, v88
	v_sub_f32_e32 v72, v72, v88
	v_sub_f32_e32 v73, v73, v88
	v_mul_f32_e32 v70, 0x3fb8aa3b, v70
	v_mul_f32_e32 v71, 0x3fb8aa3b, v71
	v_mul_f32_e32 v72, 0x3fb8aa3b, v72
	v_mul_f32_e32 v73, 0x3fb8aa3b, v73
	v_exp_f32_e32 v70, v70
	v_exp_f32_e32 v71, v71
	v_exp_f32_e32 v72, v72
	v_exp_f32_e32 v73, v73
	s_nop 0
	v_cndmask_b32_e64 v70, v70, 0, vcc
	v_cndmask_b32_e64 v71, v71, 0, vcc
	v_cndmask_b32_e64 v72, v72, 0, vcc
	v_cndmask_b32_e64 v73, v73, 0, vcc
	v_add_f32_e32 v90, v70, v71
	v_add_f32_e32 v91, v72, v73
	v_add_f32_e32 v90, v90, v91
	v_cvt_pk_bf16_f32 v92, v70, v71
	v_cvt_pk_bf16_f32 v93, v72, v73
	v_mov_b32_e32 v91, v90
	s_nop 1
	v_permlane16_swap_b32_e32 v90, v91
	v_add_f32_e32 v90, v90, v91
	v_mfma_f32_16x16x16_bf16 v[70:73], v[86:87], v[92:93], 0
	v_mov_b32_e32 v91, v90
	s_nop 1
	v_permlane32_swap_b32_e32 v90, v91
	v_add_f32_e32 v90, v90, v91
	v_rcp_f32_e32 v90, v90
	s_nop 2
	v_mul_f32_e32 v70, v70, v90
	v_mul_f32_e32 v71, v71, v90
	v_mul_f32_e32 v72, v72, v90
	v_mul_f32_e32 v73, v73, v90
	v_cvt_pk_bf16_f32 v92, v70, v71
	v_cvt_pk_bf16_f32 v93, v72, v73
	s_waitcnt lgkmcnt(0)
	s_nop 0
	v_mfma_f32_16x16x16_bf16 v[42:45], v[158:159], v[92:93], v[42:45]
	v_mfma_f32_16x16x16_bf16 v[50:53], v[160:161], v[92:93], v[50:53]
	v_mfma_f32_16x16x16_bf16 v[58:61], v[162:163], v[92:93], v[58:61]
	v_mfma_f32_16x16x16_bf16 v[66:69], v[64:65], v[92:93], v[66:69]
	s_nop 1
	s_nop 3
	v_pk_add_f32 v[120:121], v[42:43], v[84:85]
	v_pk_add_f32 v[122:123], v[44:45], v[0:1]
	v_mul_f32_e32 v1, v130, v120
	v_mul_f32_e32 v0, v120, v1
	v_mul_f32_e32 v31, v130, v121
	v_pk_add_f32 v[0:1], v[0:1], 0 op_sel_hi:[1,0]
	v_mul_f32_e32 v30, v121, v31
	v_pk_add_f32 v[0:1], v[0:1], v[30:31]
	v_mul_f32_e32 v31, v130, v122
	v_mul_f32_e32 v30, v122, v31
	v_pk_add_f32 v[0:1], v[0:1], v[30:31]
	v_mul_f32_e32 v31, v130, v123
	v_pk_add_f32 v[118:119], v[50:51], v[118:119]
	v_mul_f32_e32 v30, v123, v31
	v_pk_add_f32 v[0:1], v[0:1], v[30:31]
	v_mul_f32_e32 v31, v130, v118
	v_mul_f32_e32 v30, v118, v31
	v_pk_add_f32 v[124:125], v[52:53], v[124:125]
	v_pk_add_f32 v[0:1], v[0:1], v[30:31]
	v_mul_f32_e32 v31, v130, v119
	v_mul_f32_e32 v30, v119, v31
	v_mul_f32_e32 v33, v130, v124
	v_pk_add_f32 v[116:117], v[58:59], v[116:117]
	v_mul_f32_e32 v32, v124, v33
	v_mul_f32_e32 v35, v130, v125
	v_pk_add_f32 v[0:1], v[0:1], v[30:31]
	v_mul_f32_e32 v34, v125, v35
	v_mul_f32_e32 v37, v130, v116
	v_pk_add_f32 v[0:1], v[0:1], v[32:33]
	v_pk_add_f32 v[114:115], v[60:61], v[114:115]
	v_mul_f32_e32 v36, v116, v37
	v_mul_f32_e32 v39, v130, v117
	v_pk_add_f32 v[0:1], v[0:1], v[34:35]
	v_mul_f32_e32 v38, v117, v39
	v_mul_f32_e32 v41, v130, v114
	v_pk_add_f32 v[0:1], v[0:1], v[36:37]
	v_pk_add_f32 v[110:111], v[66:67], v[110:111]
	v_mul_f32_e32 v40, v114, v41
	v_mul_f32_e32 v43, v130, v115
	v_pk_add_f32 v[0:1], v[0:1], v[38:39]
	v_mul_f32_e32 v42, v115, v43
	v_mul_f32_e32 v45, v130, v110
	v_pk_add_f32 v[0:1], v[0:1], v[40:41]
	v_pk_add_f32 v[112:113], v[68:69], v[112:113]
	v_mul_f32_e32 v44, v110, v45
	v_mul_f32_e32 v47, v130, v111
	v_pk_add_f32 v[0:1], v[0:1], v[42:43]
	v_mul_f32_e32 v46, v111, v47
	v_mul_f32_e32 v49, v130, v112
	v_pk_add_f32 v[0:1], v[0:1], v[44:45]
	v_mul_f32_e32 v48, v112, v49
	v_pk_add_f32 v[0:1], v[0:1], v[46:47]
	v_mul_f32_e32 v31, v130, v113
	v_pk_add_f32 v[0:1], v[0:1], v[48:49]
	v_mul_f32_e32 v30, v113, v31
	v_pk_add_f32 v[0:1], v[0:1], v[30:31]
	s_branch .LBB5_139
